# speedup vs baseline: 1.0224x; 1.0224x over previous
.LBB1_3:
	s_mov_b32 s29, s16
	v_add_u32_e32 v0, s29, v101
	ds_read_b128 v[94:97], v0 offset:16384
	ds_read_b128 v[102:105], v0 offset:17408
	ds_read_b128 v[106:109], v0 offset:18432
	ds_read_b128 v[110:113], v0 offset:19456
	ds_read_b128 v[114:117], v0 offset:32768
	ds_read_b128 v[118:121], v0 offset:33792
	ds_read_b128 v[122:125], v0 offset:34816
	ds_read_b128 v[126:129], v0 offset:35840
	v_add_u32_e32 v0, s29, v91
	ds_read_b128 v[130:133], v0
	ds_read_b128 v[134:137], v0 offset:1024
	ds_read_b128 v[138:141], v0 offset:2048
	ds_read_b128 v[142:145], v0 offset:3072
	ds_read_b128 v[146:149], v0 offset:4096
	ds_read_b128 v[150:153], v0 offset:5120
	ds_read_b128 v[154:157], v0 offset:6144
	ds_read_b128 v[158:161], v0 offset:7168
	s_lshl_b32 s16, s28, 2
	s_or_b32 s16, s16, s23
	s_lshl_b64 s[30:31], s[16:17], 19
	s_add_u32 s16, s6, s30
	s_addc_u32 s31, s7, s31
	s_lshl_b32 s33, s3, 7
	s_ashr_i32 s35, s33, 31
	s_add_u32 s30, s16, s33
	s_addc_u32 s31, s31, s35
	s_add_u32 s34, s4, s33
	s_addc_u32 s35, s5, s35
	s_add_i32 s16, s19, s27
	v_lshl_add_u64 v[98:99], s[30:31], 0, v[84:85]
	s_add_i32 m0, s16, 0x4000
	s_nop 0
	global_load_lds_dwordx4 v[98:99], off
	v_lshl_add_u64 v[98:99], s[30:31], 0, v[88:89]
	s_add_i32 m0, s16, 0x6000
	s_nop 0
	global_load_lds_dwordx4 v[98:99], off
	v_lshl_add_u64 v[98:99], s[34:35], 0, v[82:83]
	s_mov_b32 m0, s16
	s_nop 0
	global_load_lds_dwordx4 v[98:99], off
	s_waitcnt vmcnt(3)
	s_waitcnt lgkmcnt(0)
	s_barrier
	s_setprio 1
	s_waitcnt lgkmcnt(0)
	v_mfma_f32_16x16x32_f16 v[78:81], v[94:97], v[130:133], v[78:81]
	v_mfma_f32_16x16x32_f16 v[74:77], v[106:109], v[130:133], v[74:77]
	v_mfma_f32_16x16x32_f16 v[66:69], v[94:97], v[138:141], v[66:69]
	v_mfma_f32_16x16x32_f16 v[58:61], v[106:109], v[138:141], v[58:61]
	v_mfma_f32_16x16x32_f16 v[78:81], v[102:105], v[134:137], v[78:81]
	v_mfma_f32_16x16x32_f16 v[74:77], v[110:113], v[134:137], v[74:77]
	v_mfma_f32_16x16x32_f16 v[66:69], v[102:105], v[142:145], v[66:69]
	v_mfma_f32_16x16x32_f16 v[58:61], v[110:113], v[142:145], v[58:61]
	s_add_u32 s30, s30, 0x40000
	s_addc_u32 s31, s31, 0
	v_lshl_add_u64 v[98:99], s[30:31], 0, v[84:85]
	s_add_i32 m0, s16, 0x8000
	s_nop 0
	global_load_lds_dwordx4 v[98:99], off
	v_mfma_f32_16x16x32_f16 v[54:57], v[94:97], v[146:149], v[54:57]
	v_mfma_f32_16x16x32_f16 v[46:49], v[106:109], v[146:149], v[46:49]
	v_mfma_f32_16x16x32_f16 v[34:37], v[94:97], v[154:157], v[34:37]
	v_mfma_f32_16x16x32_f16 v[26:29], v[106:109], v[154:157], v[26:29]
	v_mfma_f32_16x16x32_f16 v[54:57], v[102:105], v[150:153], v[54:57]
	v_mfma_f32_16x16x32_f16 v[46:49], v[110:113], v[150:153], v[46:49]
	v_mfma_f32_16x16x32_f16 v[34:37], v[102:105], v[158:161], v[34:37]
	v_mfma_f32_16x16x32_f16 v[26:29], v[110:113], v[158:161], v[26:29]
	v_lshl_add_u64 v[94:95], s[30:31], 0, v[88:89]
	s_add_i32 m0, s16, 0xa000
	s_nop 0
	global_load_lds_dwordx4 v[94:95], off
	v_mfma_f32_16x16x32_f16 v[70:73], v[114:117], v[130:133], v[70:73]
	v_mfma_f32_16x16x32_f16 v[62:65], v[122:125], v[130:133], v[62:65]
	v_mfma_f32_16x16x32_f16 v[50:53], v[114:117], v[138:141], v[50:53]
	v_mfma_f32_16x16x32_f16 v[42:45], v[122:125], v[138:141], v[42:45]
	v_mfma_f32_16x16x32_f16 v[70:73], v[118:121], v[134:137], v[70:73]
	v_mfma_f32_16x16x32_f16 v[62:65], v[126:129], v[134:137], v[62:65]
	v_mfma_f32_16x16x32_f16 v[50:53], v[118:121], v[142:145], v[50:53]
	v_mfma_f32_16x16x32_f16 v[42:45], v[126:129], v[142:145], v[42:45]
	v_lshl_add_u64 v[94:95], s[34:35], 0, v[86:87]
	s_add_i32 m0, s16, 0x2000
	s_nop 0
	global_load_lds_dwordx4 v[94:95], off
	v_mfma_f32_16x16x32_f16 v[38:41], v[114:117], v[146:149], v[38:41]
	v_mfma_f32_16x16x32_f16 v[30:33], v[122:125], v[146:149], v[30:33]
	v_mfma_f32_16x16x32_f16 v[22:25], v[114:117], v[154:157], v[22:25]
	v_mfma_f32_16x16x32_f16 v[2:5], v[122:125], v[154:157], v[2:5]
	v_mfma_f32_16x16x32_f16 v[38:41], v[118:121], v[150:153], v[38:41]
	v_mfma_f32_16x16x32_f16 v[30:33], v[126:129], v[150:153], v[30:33]
	v_mfma_f32_16x16x32_f16 v[22:25], v[118:121], v[158:161], v[22:25]
	v_mfma_f32_16x16x32_f16 v[2:5], v[126:129], v[158:161], v[2:5]
	s_setprio 0
	s_add_i32 s3, s3, 1
	s_cmp_lt_u32 s28, 2
	s_cselect_b64 s[30:31], -1, 0
	s_cmp_eq_u32 s3, 16
	s_cselect_b64 s[34:35], -1, 0
	s_and_b64 s[36:37], s[34:35], exec
	s_cselect_b32 s3, 0, s3
	s_and_b64 s[30:31], s[34:35], s[30:31]
	s_cmp_lg_u64 s[30:31], 0
	s_addc_u32 s28, s28, 0
	s_barrier
	s_add_i32 s26, s26, -1
	s_mov_b32 s16, s24
	s_mov_b32 s24, s27
	s_cmp_lg_u32 s26, 0
	s_mov_b32 s27, s29
	s_cbranch_scc1 .LBB1_3
	s_lshl_b32 s3, s14, 7
	s_add_i32 s17, s25, s3
	s_ashr_i32 s3, s17, 1
	s_lshr_b32 s14, s17, 5
	s_or_b32 s24, s15, s2
	s_and_b32 s14, s14, 62
	s_and_b32 s27, s3, 0xfffffc00
	v_or_b32_e32 v105, s24, v1
	v_lshlrev_b32_e32 v98, 4, v93
	v_or_b32_e32 v102, 16, v93
	v_or_b32_e32 v103, 32, v93
	v_or_b32_e32 v104, 48, v93
	v_mov_b32_e32 v93, 0
	s_and_b32 s16, s24, 0x340
	v_lshlrev_b32_e32 v95, 6, v105
	s_or_b32 s2, s27, s14
	v_lshlrev_b32_e32 v0, 9, v92
	v_and_b32_e32 v110, 0xc00, v95
	v_mov_b32_e32 v111, v93
	s_or_b32 s14, s2, s16
	v_and_b32_e32 v92, 0x200, v0
	v_lshl_add_u64 v[110:111], s[8:9], 0, v[110:111]
	s_or_b32 s30, s14, 0x80
	s_mov_b32 s3, 0
	v_mov_b32_e32 v99, v93
	v_lshl_add_u64 v[110:111], v[110:111], 0, v[92:93]
	s_mov_b32 s2, 0x3e38aa3b
	v_pk_add_f32 v[72:73], v[12:13], v[72:73]
	v_pk_add_f32 v[70:71], v[10:11], v[70:71]
	v_pk_add_f32 v[64:65], v[8:9], v[64:65]
	v_pk_add_f32 v[62:63], v[6:7], v[62:63]
	s_ashr_i32 s31, s30, 31
	v_lshl_add_u64 v[112:113], v[110:111], 0, v[98:99]
	v_pk_mul_f32 v[72:73], v[72:73], s[2:3] op_sel_hi:[1,0]
	v_pk_mul_f32 v[70:71], v[70:71], s[2:3] op_sel_hi:[1,0]
	v_pk_mul_f32 v[64:65], v[64:65], s[2:3] op_sel_hi:[1,0]
	v_pk_mul_f32 v[62:63], v[62:63], s[2:3] op_sel_hi:[1,0]
	s_lshl_b64 s[30:31], s[30:31], 12
	v_lshlrev_b32_e32 v96, 4, v102
	v_mov_b32_e32 v97, v93
	v_pk_add_f32 v[80:81], v[20:21], v[80:81]
	v_pk_add_f32 v[78:79], v[18:19], v[78:79]
	v_pk_add_f32 v[74:75], v[14:15], v[74:75]
	s_ashr_i32 s15, s14, 31
	v_cvt_pk_f16_f32 v70, v70, v71
	v_cvt_pk_f16_f32 v71, v72, v73
	v_cvt_pk_f16_f32 v72, v62, v63
	v_cvt_pk_f16_f32 v73, v64, v65
	v_lshl_add_u64 v[62:63], v[112:113], 0, s[30:31]
	v_pk_add_f32 v[58:59], v[14:15], v[58:59]
	v_pk_mul_f32 v[80:81], v[80:81], s[2:3] op_sel_hi:[1,0]
	v_pk_mul_f32 v[78:79], v[78:79], s[2:3] op_sel_hi:[1,0]
	v_pk_mul_f32 v[74:75], v[74:75], s[2:3] op_sel_hi:[1,0]
	s_lshl_b64 s[28:29], s[14:15], 12
	global_store_dwordx4 v[62:63], v[70:73], off sc1
	v_pk_add_f32 v[62:63], v[20:21], v[68:69]
	v_pk_add_f32 v[64:65], v[18:19], v[66:67]
	v_lshl_add_u64 v[70:71], v[110:111], 0, v[96:97]
	v_pk_mul_f32 v[58:59], v[58:59], s[2:3] op_sel_hi:[1,0]
	v_pk_add_f32 v[52:53], v[12:13], v[52:53]
	v_pk_add_f32 v[50:51], v[10:11], v[50:51]
	v_pk_add_f32 v[44:45], v[8:9], v[44:45]
	v_pk_add_f32 v[42:43], v[6:7], v[42:43]
	v_lshlrev_b32_e32 v0, 4, v103
	v_cvt_pk_f16_f32 v78, v78, v79
	v_cvt_pk_f16_f32 v79, v80, v81
	v_cvt_pk_f16_f32 v80, v74, v75
	v_lshl_add_u64 v[74:75], v[112:113], 0, s[28:29]
	v_pk_mul_f32 v[66:67], v[62:63], s[2:3] op_sel_hi:[1,0]
	v_pk_mul_f32 v[62:63], v[64:65], s[2:3] op_sel_hi:[1,0]
	v_cvt_pk_f16_f32 v64, v58, v59
	v_lshl_add_u64 v[58:59], v[70:71], 0, s[28:29]
	v_pk_mul_f32 v[52:53], v[52:53], s[2:3] op_sel_hi:[1,0]
	v_pk_mul_f32 v[50:51], v[50:51], s[2:3] op_sel_hi:[1,0]
	v_pk_mul_f32 v[44:45], v[44:45], s[2:3] op_sel_hi:[1,0]
	v_pk_mul_f32 v[42:43], v[42:43], s[2:3] op_sel_hi:[1,0]
	s_or_b32 s28, s14, 1
	s_or_b32 s14, s14, 0x81
	v_and_b32_e32 v106, 0xf0, v0
	v_mov_b32_e32 v107, v93
	v_cvt_pk_f16_f32 v50, v50, v51
	v_cvt_pk_f16_f32 v51, v52, v53
	v_cvt_pk_f16_f32 v52, v42, v43
	v_cvt_pk_f16_f32 v53, v44, v45
	v_lshl_add_u64 v[42:43], v[70:71], 0, s[30:31]
	v_pk_add_f32 v[40:41], v[12:13], v[40:41]
	v_pk_add_f32 v[38:39], v[10:11], v[38:39]
	v_pk_add_f32 v[32:33], v[8:9], v[32:33]
	v_pk_add_f32 v[30:31], v[6:7], v[30:31]
	s_ashr_i32 s15, s14, 31
	v_lshlrev_b32_e32 v94, 4, v104
	global_store_dwordx4 v[42:43], v[50:53], off sc1
	v_pk_mul_f32 v[40:41], v[40:41], s[2:3] op_sel_hi:[1,0]
	v_pk_mul_f32 v[38:39], v[38:39], s[2:3] op_sel_hi:[1,0]
	v_lshl_add_u64 v[50:51], v[110:111], 0, v[106:107]
	v_pk_mul_f32 v[32:33], v[32:33], s[2:3] op_sel_hi:[1,0]
	v_pk_mul_f32 v[30:31], v[30:31], s[2:3] op_sel_hi:[1,0]
	s_lshl_b64 s[14:15], s[14:15], 12
	v_and_b32_e32 v108, 0x1f0, v94
	v_mov_b32_e32 v109, v93
	v_pk_add_f32 v[42:43], v[20:21], v[56:57]
	v_pk_add_f32 v[44:45], v[18:19], v[54:55]
	v_pk_add_f32 v[46:47], v[14:15], v[46:47]
	s_ashr_i32 s29, s28, 31
	v_cvt_pk_f16_f32 v38, v38, v39
	v_cvt_pk_f16_f32 v39, v40, v41
	v_cvt_pk_f16_f32 v40, v30, v31
	v_cvt_pk_f16_f32 v41, v32, v33
	v_lshl_add_u64 v[30:31], v[50:51], 0, s[14:15]
	v_pk_add_f32 v[20:21], v[20:21], v[36:37]
	v_pk_add_f32 v[18:19], v[18:19], v[34:35]
	v_pk_add_f32 v[14:15], v[14:15], v[26:27]
	v_pk_add_f32 v[76:77], v[16:17], v[76:77]
	v_pk_add_f32 v[60:61], v[16:17], v[60:61]
	v_pk_mul_f32 v[52:53], v[42:43], s[2:3] op_sel_hi:[1,0]
	v_pk_mul_f32 v[42:43], v[44:45], s[2:3] op_sel_hi:[1,0]
	v_pk_add_f32 v[44:45], v[16:17], v[48:49]
	s_lshl_b64 s[28:29], s[28:29], 12
	global_store_dwordx4 v[30:31], v[38:41], off sc1
	v_lshl_add_u64 v[30:31], v[110:111], 0, v[108:109]
	v_pk_mul_f32 v[20:21], v[20:21], s[2:3] op_sel_hi:[1,0]
	v_pk_mul_f32 v[18:19], v[18:19], s[2:3] op_sel_hi:[1,0]
	v_pk_add_f32 v[16:17], v[16:17], v[28:29]
	v_pk_mul_f32 v[14:15], v[14:15], s[2:3] op_sel_hi:[1,0]
	v_pk_add_f32 v[12:13], v[12:13], v[24:25]
	v_pk_add_f32 v[10:11], v[10:11], v[22:23]
	v_pk_add_f32 v[4:5], v[8:9], v[4:5]
	v_pk_add_f32 v[2:3], v[6:7], v[2:3]
	v_pk_mul_f32 v[76:77], v[76:77], s[2:3] op_sel_hi:[1,0]
	v_pk_mul_f32 v[60:61], v[60:61], s[2:3] op_sel_hi:[1,0]
	v_pk_mul_f32 v[48:49], v[44:45], s[2:3] op_sel_hi:[1,0]
	v_pk_mul_f32 v[44:45], v[46:47], s[2:3] op_sel_hi:[1,0]
	v_lshl_add_u64 v[46:47], v[50:51], 0, s[28:29]
	v_cvt_pk_f16_f32 v18, v18, v19
	v_cvt_pk_f16_f32 v19, v20, v21
	v_pk_mul_f32 v[16:17], v[16:17], s[2:3] op_sel_hi:[1,0]
	v_cvt_pk_f16_f32 v20, v14, v15
	v_lshl_add_u64 v[14:15], v[30:31], 0, s[28:29]
	v_pk_mul_f32 v[12:13], v[12:13], s[2:3] op_sel_hi:[1,0]
	v_pk_mul_f32 v[10:11], v[10:11], s[2:3] op_sel_hi:[1,0]
	v_pk_mul_f32 v[4:5], v[4:5], s[2:3] op_sel_hi:[1,0]
	v_pk_mul_f32 v[2:3], v[2:3], s[2:3] op_sel_hi:[1,0]
	s_add_u32 s28, s20, s22
	v_cvt_pk_f16_f32 v81, v76, v77
	v_cvt_pk_f16_f32 v62, v62, v63
	v_cvt_pk_f16_f32 v63, v66, v67
	v_cvt_pk_f16_f32 v65, v60, v61
	v_cvt_pk_f16_f32 v42, v42, v43
	v_cvt_pk_f16_f32 v43, v52, v53
	v_cvt_pk_f16_f32 v44, v44, v45
	v_cvt_pk_f16_f32 v45, v48, v49
	v_cvt_pk_f16_f32 v21, v16, v17
	v_cvt_pk_f16_f32 v10, v10, v11
	v_cvt_pk_f16_f32 v11, v12, v13
	v_cvt_pk_f16_f32 v12, v2, v3
	v_cvt_pk_f16_f32 v13, v4, v5
	v_lshl_add_u64 v[2:3], v[30:31], 0, s[14:15]
	s_addc_u32 s29, s21, 0
	v_lshlrev_b32_e32 v92, 2, v1
	global_store_dwordx4 v[74:75], v[78:81], off sc1
	global_store_dwordx4 v[58:59], v[62:65], off sc1
	global_store_dwordx4 v[46:47], v[42:45], off sc1
	global_store_dwordx4 v[14:15], v[18:21], off sc1
	global_store_dwordx4 v[2:3], v[10:13], off sc1
	v_lshl_add_u64 v[2:3], s[28:29], 0, v[92:93]
	s_mov_b64 s[28:29], 0x1000
	v_lshl_add_u64 v[10:11], v[2:3], 0, s[28:29]
	global_load_dwordx4 v[22:25], v[10:11], off
	global_load_dwordx4 v[14:17], v[10:11], off offset:16
	global_load_dwordx4 v[6:9], v[10:11], off offset:512
	global_load_dwordx4 v[2:5], v[10:11], off offset:528
	s_mov_b32 s25, 1
	s_mov_b32 s26, 16
	s_mov_b32 s14, 2
	s_mov_b32 s15, 0x18000
	s_mov_b32 s2, 0xc000
	s_mov_b32 s27, 0
	v_mov_b32_e32 v10, v93
	v_mov_b32_e32 v11, v93
	v_mov_b32_e32 v12, v93
	v_mov_b32_e32 v13, v93
	v_mov_b32_e32 v18, v93
	v_mov_b32_e32 v19, v93
	v_mov_b32_e32 v20, v93
	v_mov_b32_e32 v21, v93
	v_mov_b32_e32 v26, v93
	v_mov_b32_e32 v27, v93
	v_mov_b32_e32 v28, v93
	v_mov_b32_e32 v29, v93
	v_mov_b32_e32 v34, v93
	v_mov_b32_e32 v35, v93
	v_mov_b32_e32 v36, v93
	v_mov_b32_e32 v37, v93
	v_mov_b32_e32 v42, v93
	v_mov_b32_e32 v43, v93
	v_mov_b32_e32 v44, v93
	v_mov_b32_e32 v45, v93
	v_mov_b32_e32 v50, v93
	v_mov_b32_e32 v51, v93
	v_mov_b32_e32 v52, v93
	v_mov_b32_e32 v53, v93
	v_mov_b32_e32 v62, v93
	v_mov_b32_e32 v63, v93
	v_mov_b32_e32 v64, v93
	v_mov_b32_e32 v65, v93
	v_mov_b32_e32 v70, v93
	v_mov_b32_e32 v71, v93
	v_mov_b32_e32 v72, v93
	v_mov_b32_e32 v73, v93
	v_mov_b32_e32 v30, v93
	v_mov_b32_e32 v31, v93
	v_mov_b32_e32 v32, v93
	v_mov_b32_e32 v33, v93
	v_mov_b32_e32 v38, v93
	v_mov_b32_e32 v39, v93
	v_mov_b32_e32 v40, v93
	v_mov_b32_e32 v41, v93
	v_mov_b32_e32 v46, v93
	v_mov_b32_e32 v47, v93
	v_mov_b32_e32 v48, v93
	v_mov_b32_e32 v49, v93
	v_mov_b32_e32 v54, v93
	v_mov_b32_e32 v55, v93
	v_mov_b32_e32 v56, v93
	v_mov_b32_e32 v57, v93
	v_mov_b32_e32 v58, v93
	v_mov_b32_e32 v59, v93
	v_mov_b32_e32 v60, v93
	v_mov_b32_e32 v61, v93
	v_mov_b32_e32 v66, v93
	v_mov_b32_e32 v67, v93
	v_mov_b32_e32 v68, v93
	v_mov_b32_e32 v69, v93
	v_mov_b32_e32 v74, v93
	v_mov_b32_e32 v75, v93
	v_mov_b32_e32 v76, v93
	v_mov_b32_e32 v77, v93
	v_mov_b32_e32 v78, v93
	v_mov_b32_e32 v79, v93
	v_mov_b32_e32 v80, v93
	v_mov_b32_e32 v81, v93
.LBB1_5:
	s_mov_b32 s28, s2
	v_add_u32_e32 v1, s28, v101
	ds_read_b128 v[106:109], v1 offset:16384
	ds_read_b128 v[110:113], v1 offset:17408
	ds_read_b128 v[114:117], v1 offset:18432
	ds_read_b128 v[118:121], v1 offset:19456
	ds_read_b128 v[122:125], v1 offset:32768
	ds_read_b128 v[126:129], v1 offset:33792
	ds_read_b128 v[130:133], v1 offset:34816
	ds_read_b128 v[134:137], v1 offset:35840
	v_add_u32_e32 v1, s28, v91
	ds_read_b128 v[138:141], v1
	ds_read_b128 v[142:145], v1 offset:1024
	ds_read_b128 v[146:149], v1 offset:2048
	ds_read_b128 v[150:153], v1 offset:3072
	ds_read_b128 v[154:157], v1 offset:4096
	ds_read_b128 v[158:161], v1 offset:5120
	ds_read_b128 v[162:165], v1 offset:6144
	ds_read_b128 v[166:169], v1 offset:7168
	s_lshl_b32 s2, s25, 2
	s_or_b32 s2, s2, s23
	s_lshl_b64 s[30:31], s[2:3], 19
	s_add_u32 s2, s6, s30
	s_addc_u32 s29, s7, s31
	s_lshl_b32 s33, s14, 7
	s_ashr_i32 s35, s33, 31
	s_add_u32 s30, s2, s33
	s_addc_u32 s31, s29, s35
	s_add_u32 s34, s4, s33
	s_addc_u32 s35, s5, s35
	s_add_i32 s2, s19, s27
	v_lshl_add_u64 v[170:171], s[30:31], 0, v[84:85]
	s_add_i32 m0, s2, 0x4000
	s_nop 0
	global_load_lds_dwordx4 v[170:171], off
	v_lshl_add_u64 v[170:171], s[30:31], 0, v[88:89]
	s_add_i32 m0, s2, 0x6000
	s_nop 0
	global_load_lds_dwordx4 v[170:171], off
	v_lshl_add_u64 v[170:171], s[34:35], 0, v[82:83]
	s_mov_b32 m0, s2
	s_nop 0
	global_load_lds_dwordx4 v[170:171], off
	s_waitcnt vmcnt(3)
	s_waitcnt lgkmcnt(0)
	s_barrier
	s_setprio 1
	s_waitcnt lgkmcnt(0)
	v_mfma_f32_16x16x32_f16 v[78:81], v[106:109], v[138:141], v[78:81]
	v_mfma_f32_16x16x32_f16 v[74:77], v[114:117], v[138:141], v[74:77]
	v_mfma_f32_16x16x32_f16 v[66:69], v[106:109], v[146:149], v[66:69]
	v_mfma_f32_16x16x32_f16 v[58:61], v[114:117], v[146:149], v[58:61]
	v_mfma_f32_16x16x32_f16 v[78:81], v[110:113], v[142:145], v[78:81]
	v_mfma_f32_16x16x32_f16 v[74:77], v[118:121], v[142:145], v[74:77]
	v_mfma_f32_16x16x32_f16 v[66:69], v[110:113], v[150:153], v[66:69]
	v_mfma_f32_16x16x32_f16 v[58:61], v[118:121], v[150:153], v[58:61]
	s_add_u32 s30, s30, 0x40000
	s_addc_u32 s31, s31, 0
	v_lshl_add_u64 v[170:171], s[30:31], 0, v[84:85]
	s_add_i32 m0, s2, 0x8000
	s_nop 0
	global_load_lds_dwordx4 v[170:171], off
	v_mfma_f32_16x16x32_f16 v[54:57], v[106:109], v[154:157], v[54:57]
	v_mfma_f32_16x16x32_f16 v[46:49], v[114:117], v[154:157], v[46:49]
	v_mfma_f32_16x16x32_f16 v[38:41], v[106:109], v[162:165], v[38:41]
	v_mfma_f32_16x16x32_f16 v[30:33], v[114:117], v[162:165], v[30:33]
	v_mfma_f32_16x16x32_f16 v[54:57], v[110:113], v[158:161], v[54:57]
	v_mfma_f32_16x16x32_f16 v[46:49], v[118:121], v[158:161], v[46:49]
	v_mfma_f32_16x16x32_f16 v[38:41], v[110:113], v[166:169], v[38:41]
	v_mfma_f32_16x16x32_f16 v[30:33], v[118:121], v[166:169], v[30:33]
	v_lshl_add_u64 v[106:107], s[30:31], 0, v[88:89]
	s_add_i32 m0, s2, 0xa000
	s_nop 0
	global_load_lds_dwordx4 v[106:107], off
	v_mfma_f32_16x16x32_f16 v[70:73], v[122:125], v[138:141], v[70:73]
	v_mfma_f32_16x16x32_f16 v[62:65], v[130:133], v[138:141], v[62:65]
	v_mfma_f32_16x16x32_f16 v[50:53], v[122:125], v[146:149], v[50:53]
	v_mfma_f32_16x16x32_f16 v[42:45], v[130:133], v[146:149], v[42:45]
	v_mfma_f32_16x16x32_f16 v[70:73], v[126:129], v[142:145], v[70:73]
	v_mfma_f32_16x16x32_f16 v[62:65], v[134:137], v[142:145], v[62:65]
	v_mfma_f32_16x16x32_f16 v[50:53], v[126:129], v[150:153], v[50:53]
	v_mfma_f32_16x16x32_f16 v[42:45], v[134:137], v[150:153], v[42:45]
	v_lshl_add_u64 v[106:107], s[34:35], 0, v[86:87]
	s_add_i32 m0, s2, 0x2000
	s_nop 0
	global_load_lds_dwordx4 v[106:107], off
	v_mfma_f32_16x16x32_f16 v[34:37], v[122:125], v[154:157], v[34:37]
	v_mfma_f32_16x16x32_f16 v[26:29], v[130:133], v[154:157], v[26:29]
	v_mfma_f32_16x16x32_f16 v[18:21], v[122:125], v[162:165], v[18:21]
	v_mfma_f32_16x16x32_f16 v[10:13], v[130:133], v[162:165], v[10:13]
	v_mfma_f32_16x16x32_f16 v[34:37], v[126:129], v[158:161], v[34:37]
	v_mfma_f32_16x16x32_f16 v[26:29], v[134:137], v[158:161], v[26:29]
	v_mfma_f32_16x16x32_f16 v[18:21], v[126:129], v[166:169], v[18:21]
	v_mfma_f32_16x16x32_f16 v[10:13], v[134:137], v[166:169], v[10:13]
	s_setprio 0
	s_add_i32 s2, s14, 1
	s_cmp_lt_u32 s25, 2
	s_cselect_b64 s[30:31], -1, 0
	s_cmp_eq_u32 s2, 16
	s_cselect_b64 s[34:35], -1, 0
	s_and_b64 s[36:37], s[34:35], exec
	s_cselect_b32 s14, 0, s2
	s_and_b64 s[30:31], s[34:35], s[30:31]
	s_cmp_lg_u64 s[30:31], 0
	s_addc_u32 s25, s25, 0
	s_barrier
	s_add_i32 s26, s26, -1
	s_mov_b32 s2, s15
	s_mov_b32 s15, s27
	s_cmp_lg_u32 s26, 0
	s_mov_b32 s27, s28
	s_cbranch_scc1 .LBB1_5
	s_ashr_i32 s2, s17, 7
	s_and_b32 s3, s2, -16
	s_or_b32 s2, s3, 2
	s_sub_u32 s14, s10, s8
	s_subb_u32 s11, s11, s9
	s_bfe_u32 s6, s17, 0x50006
	s_add_u32 s14, s8, s14
	s_addc_u32 s15, s9, s11
	s_lshr_b32 s11, s24, 6
	s_or_b32 s17, s11, s3
	s_lshl_b32 s17, s17, 8
	s_lshl_b32 s23, s6, 3
	v_bfe_u32 v93, v105, 3, 3
	v_pk_add_f32 v[80:81], v[24:25], v[80:81]
	v_pk_add_f32 v[78:79], v[22:23], v[78:79]
	v_pk_add_f32 v[74:75], v[14:15], v[74:75]
	s_or_b32 s17, s17, s23
	s_or_b32 s11, s2, s11
	v_cvt_pk_f16_f32 v78, v78, v79
	v_cvt_pk_f16_f32 v79, v80, v81
	v_cvt_pk_f16_f32 v80, v74, v75
	v_or_b32_e32 v74, s17, v93
	s_lshl_b32 s11, s11, 8
	v_ashrrev_i32_e32 v75, 31, v74
	v_pk_add_f32 v[72:73], v[8:9], v[72:73]
	v_pk_add_f32 v[70:71], v[6:7], v[70:71]
	v_pk_add_f32 v[62:63], v[2:3], v[62:63]
	s_or_b32 s11, s11, s23
	v_lshlrev_b64 v[74:75], 10, v[74:75]
	v_cvt_pk_f16_f32 v70, v70, v71
	v_cvt_pk_f16_f32 v71, v72, v73
	v_cvt_pk_f16_f32 v72, v62, v63
	v_or_b32_e32 v62, s11, v93
	v_pk_add_f32 v[76:77], v[16:17], v[76:77]
	v_lshl_add_u64 v[74:75], s[14:15], 0, v[74:75]
	v_ashrrev_i32_e32 v63, 31, v62
	v_cvt_pk_f16_f32 v81, v76, v77
	v_lshl_add_u64 v[76:77], v[74:75], 0, v[98:99]
	v_lshlrev_b64 v[62:63], 10, v[62:63]
	global_store_dwordx4 v[76:77], v[78:81], off sc1
	v_pk_add_f32 v[64:65], v[4:5], v[64:65]
	v_lshl_add_u64 v[76:77], s[14:15], 0, v[62:63]
	v_cvt_pk_f16_f32 v73, v64, v65
	v_lshl_add_u64 v[62:63], v[76:77], 0, v[98:99]
	global_store_dwordx4 v[62:63], v[70:73], off sc1
	v_pk_add_f32 v[64:65], v[24:25], v[68:69]
	v_pk_add_f32 v[62:63], v[22:23], v[66:67]
	v_pk_add_f32 v[60:61], v[16:17], v[60:61]
	v_pk_add_f32 v[58:59], v[14:15], v[58:59]
	v_pk_add_f32 v[52:53], v[8:9], v[52:53]
	v_pk_add_f32 v[50:51], v[6:7], v[50:51]
	v_pk_add_f32 v[44:45], v[4:5], v[44:45]
	v_pk_add_f32 v[42:43], v[2:3], v[42:43]
	v_cvt_pk_f16_f32 v62, v62, v63
	v_cvt_pk_f16_f32 v63, v64, v65
	v_cvt_pk_f16_f32 v64, v58, v59
	v_cvt_pk_f16_f32 v65, v60, v61
	v_lshl_add_u64 v[58:59], v[74:75], 0, v[96:97]
	v_cvt_pk_f16_f32 v50, v50, v51
	v_cvt_pk_f16_f32 v51, v52, v53
	v_cvt_pk_f16_f32 v52, v42, v43
	v_cvt_pk_f16_f32 v53, v44, v45
	v_lshl_add_u64 v[42:43], v[76:77], 0, v[96:97]
	v_mov_b32_e32 v1, 0
	global_store_dwordx4 v[58:59], v[62:65], off sc1
	global_store_dwordx4 v[42:43], v[50:53], off sc1
	v_pk_add_f32 v[44:45], v[24:25], v[56:57]
	v_pk_add_f32 v[42:43], v[22:23], v[54:55]
	v_mov_b32_e32 v95, v1
	v_cvt_pk_f16_f32 v42, v42, v43
	v_cvt_pk_f16_f32 v43, v44, v45
	v_pk_add_f32 v[48:49], v[16:17], v[48:49]
	v_pk_add_f32 v[44:45], v[14:15], v[46:47]
	v_pk_add_f32 v[36:37], v[8:9], v[36:37]
	v_pk_add_f32 v[34:35], v[6:7], v[34:35]
	v_pk_add_f32 v[28:29], v[4:5], v[28:29]
	v_pk_add_f32 v[26:27], v[2:3], v[26:27]
	v_pk_add_f32 v[24:25], v[24:25], v[40:41]
	v_pk_add_f32 v[22:23], v[22:23], v[38:39]
	v_pk_add_f32 v[16:17], v[16:17], v[32:33]
	v_pk_add_f32 v[14:15], v[14:15], v[30:31]
	v_pk_add_f32 v[8:9], v[8:9], v[20:21]
	v_pk_add_f32 v[6:7], v[6:7], v[18:19]
	v_pk_add_f32 v[4:5], v[4:5], v[12:13]
	v_pk_add_f32 v[2:3], v[2:3], v[10:11]
	s_add_u32 s14, s20, s22
	v_cvt_pk_f16_f32 v44, v44, v45
	v_cvt_pk_f16_f32 v45, v48, v49
	v_lshl_add_u64 v[46:47], v[74:75], 0, v[0:1]
	v_cvt_pk_f16_f32 v34, v34, v35
	v_cvt_pk_f16_f32 v35, v36, v37
	v_cvt_pk_f16_f32 v36, v26, v27
	v_cvt_pk_f16_f32 v37, v28, v29
	v_lshl_add_u64 v[26:27], v[76:77], 0, v[0:1]
	v_cvt_pk_f16_f32 v22, v22, v23
	v_cvt_pk_f16_f32 v23, v24, v25
	v_cvt_pk_f16_f32 v24, v14, v15
	v_cvt_pk_f16_f32 v25, v16, v17
	v_lshl_add_u64 v[14:15], v[74:75], 0, v[94:95]
	v_cvt_pk_f16_f32 v6, v6, v7
	v_cvt_pk_f16_f32 v7, v8, v9
	v_cvt_pk_f16_f32 v8, v2, v3
	v_cvt_pk_f16_f32 v9, v4, v5
	v_lshl_add_u64 v[2:3], v[76:77], 0, v[94:95]
	s_addc_u32 s15, s21, 0
	v_mov_b32_e32 v93, v1
	global_store_dwordx4 v[46:47], v[42:45], off sc1
	global_store_dwordx4 v[26:27], v[34:37], off sc1
	global_store_dwordx4 v[14:15], v[22:25], off sc1
	global_store_dwordx4 v[2:3], v[6:9], off sc1
	v_lshl_add_u64 v[2:3], s[14:15], 0, v[92:93]
	s_mov_b64 s[14:15], 0x2000
	v_lshl_add_u64 v[2:3], v[2:3], 0, s[14:15]
	global_load_dwordx4 v[20:23], v[2:3], off
	global_load_dwordx4 v[12:15], v[2:3], off offset:16
	global_load_dwordx4 v[8:11], v[2:3], off offset:512
	global_load_dwordx4 v[4:7], v[2:3], off offset:528
	s_add_u32 s11, s12, 0x400000
	s_mov_b32 s7, 2
	v_and_b32_e32 v106, 56, v105
	s_mov_b32 s10, 0
	s_addc_u32 s12, s13, 0
	s_mov_b32 s14, 0xc000
	s_mov_b32 s17, 0x18000
	s_mov_b32 s13, 16
	v_mov_b32_e32 v0, v1
	v_mov_b32_e32 v2, v1
	v_mov_b32_e32 v3, v1
	v_mov_b32_e32 v16, v1
	v_mov_b32_e32 v17, v1
	v_mov_b32_e32 v18, v1
	v_mov_b32_e32 v19, v1
	v_mov_b32_e32 v24, v1
	v_mov_b32_e32 v25, v1
	v_mov_b32_e32 v26, v1
	v_mov_b32_e32 v27, v1
	v_mov_b32_e32 v32, v1
	v_mov_b32_e32 v33, v1
	v_mov_b32_e32 v34, v1
	v_mov_b32_e32 v35, v1
	v_mov_b32_e32 v40, v1
	v_mov_b32_e32 v41, v1
	v_mov_b32_e32 v42, v1
	v_mov_b32_e32 v43, v1
	v_mov_b32_e32 v48, v1
	v_mov_b32_e32 v49, v1
	v_mov_b32_e32 v50, v1
	v_mov_b32_e32 v51, v1
	v_mov_b32_e32 v60, v1
	v_mov_b32_e32 v61, v1
	v_mov_b32_e32 v62, v1
	v_mov_b32_e32 v63, v1
	v_mov_b32_e32 v68, v1
	v_mov_b32_e32 v69, v1
	v_mov_b32_e32 v70, v1
	v_mov_b32_e32 v71, v1
	v_mov_b32_e32 v28, v1
	v_mov_b32_e32 v29, v1
	v_mov_b32_e32 v30, v1
	v_mov_b32_e32 v31, v1
	v_mov_b32_e32 v36, v1
	v_mov_b32_e32 v37, v1
	v_mov_b32_e32 v38, v1
	v_mov_b32_e32 v39, v1
	v_mov_b32_e32 v44, v1
	v_mov_b32_e32 v45, v1
	v_mov_b32_e32 v46, v1
	v_mov_b32_e32 v47, v1
	v_mov_b32_e32 v52, v1
	v_mov_b32_e32 v53, v1
	v_mov_b32_e32 v54, v1
	v_mov_b32_e32 v55, v1
	v_mov_b32_e32 v56, v1
	v_mov_b32_e32 v57, v1
	v_mov_b32_e32 v58, v1
	v_mov_b32_e32 v59, v1
	v_mov_b32_e32 v64, v1
	v_mov_b32_e32 v65, v1
	v_mov_b32_e32 v66, v1
	v_mov_b32_e32 v67, v1
	v_mov_b32_e32 v72, v1
	v_mov_b32_e32 v73, v1
	v_mov_b32_e32 v74, v1
	v_mov_b32_e32 v75, v1
	v_mov_b32_e32 v76, v1
	v_mov_b32_e32 v77, v1
	v_mov_b32_e32 v78, v1
	v_mov_b32_e32 v79, v1
.LBB1_7:
	s_mov_b32 s15, s17
	v_add_u32_e32 v80, s15, v101
	ds_read_b128 v[92:95], v80 offset:16384
	ds_read_b128 v[96:99], v80 offset:17408
	ds_read_b128 v[108:111], v80 offset:18432
	ds_read_b128 v[112:115], v80 offset:19456
	ds_read_b128 v[116:119], v80 offset:32768
	ds_read_b128 v[120:123], v80 offset:33792
	ds_read_b128 v[124:127], v80 offset:34816
	ds_read_b128 v[128:131], v80 offset:35840
	v_add_u32_e32 v80, s15, v91
	ds_read_b128 v[132:135], v80
	ds_read_b128 v[136:139], v80 offset:1024
	ds_read_b128 v[140:143], v80 offset:2048
	ds_read_b128 v[144:147], v80 offset:3072
	ds_read_b128 v[148:151], v80 offset:4096
	ds_read_b128 v[152:155], v80 offset:5120
	ds_read_b128 v[156:159], v80 offset:6144
	ds_read_b128 v[160:163], v80 offset:7168
	s_lshl_b32 s17, s7, 7
	s_ashr_i32 s23, s17, 31
	s_add_u32 s20, s11, s17
	s_addc_u32 s21, s12, s23
	s_add_u32 s22, s4, s17
	s_addc_u32 s23, s5, s23
	s_add_i32 s17, s19, s14
	v_lshl_add_u64 v[80:81], s[20:21], 0, v[84:85]
	s_add_i32 m0, s17, 0x4000
	s_nop 0
	global_load_lds_dwordx4 v[80:81], off
	v_lshl_add_u64 v[80:81], s[20:21], 0, v[88:89]
	s_add_i32 m0, s17, 0x6000
	s_nop 0
	global_load_lds_dwordx4 v[80:81], off
	v_lshl_add_u64 v[80:81], s[22:23], 0, v[82:83]
	s_mov_b32 m0, s17
	s_nop 0
	global_load_lds_dwordx4 v[80:81], off
	s_waitcnt vmcnt(3)
	s_waitcnt lgkmcnt(0)
	s_barrier
	s_setprio 1
	s_waitcnt lgkmcnt(0)
	v_mfma_f32_16x16x32_f16 v[76:79], v[92:95], v[132:135], v[76:79]
	v_mfma_f32_16x16x32_f16 v[72:75], v[108:111], v[132:135], v[72:75]
	v_mfma_f32_16x16x32_f16 v[64:67], v[92:95], v[140:143], v[64:67]
	v_mfma_f32_16x16x32_f16 v[56:59], v[108:111], v[140:143], v[56:59]
	v_mfma_f32_16x16x32_f16 v[76:79], v[96:99], v[136:139], v[76:79]
	v_mfma_f32_16x16x32_f16 v[72:75], v[112:115], v[136:139], v[72:75]
	v_mfma_f32_16x16x32_f16 v[64:67], v[96:99], v[144:147], v[64:67]
	v_mfma_f32_16x16x32_f16 v[56:59], v[112:115], v[144:147], v[56:59]
	s_add_u32 s20, s20, 0x40000
	s_addc_u32 s21, s21, 0
	v_lshl_add_u64 v[80:81], s[20:21], 0, v[84:85]
	s_add_i32 m0, s17, 0x8000
	s_nop 0
	global_load_lds_dwordx4 v[80:81], off
	v_mfma_f32_16x16x32_f16 v[52:55], v[92:95], v[148:151], v[52:55]
	v_mfma_f32_16x16x32_f16 v[44:47], v[108:111], v[148:151], v[44:47]
	v_mfma_f32_16x16x32_f16 v[36:39], v[92:95], v[156:159], v[36:39]
	v_mfma_f32_16x16x32_f16 v[28:31], v[108:111], v[156:159], v[28:31]
	v_mfma_f32_16x16x32_f16 v[52:55], v[96:99], v[152:155], v[52:55]
	v_mfma_f32_16x16x32_f16 v[44:47], v[112:115], v[152:155], v[44:47]
	v_mfma_f32_16x16x32_f16 v[36:39], v[96:99], v[160:163], v[36:39]
	v_mfma_f32_16x16x32_f16 v[28:31], v[112:115], v[160:163], v[28:31]
	v_lshl_add_u64 v[80:81], s[20:21], 0, v[88:89]
	s_add_i32 m0, s17, 0xa000
	s_nop 0
	global_load_lds_dwordx4 v[80:81], off
	v_mfma_f32_16x16x32_f16 v[68:71], v[116:119], v[132:135], v[68:71]
	v_mfma_f32_16x16x32_f16 v[60:63], v[124:127], v[132:135], v[60:63]
	v_mfma_f32_16x16x32_f16 v[48:51], v[116:119], v[140:143], v[48:51]
	v_mfma_f32_16x16x32_f16 v[40:43], v[124:127], v[140:143], v[40:43]
	v_mfma_f32_16x16x32_f16 v[68:71], v[120:123], v[136:139], v[68:71]
	v_mfma_f32_16x16x32_f16 v[60:63], v[128:131], v[136:139], v[60:63]
	v_mfma_f32_16x16x32_f16 v[48:51], v[120:123], v[144:147], v[48:51]
	v_mfma_f32_16x16x32_f16 v[40:43], v[128:131], v[144:147], v[40:43]
	v_lshl_add_u64 v[80:81], s[22:23], 0, v[86:87]
	s_add_i32 m0, s17, 0x2000
	s_nop 0
	global_load_lds_dwordx4 v[80:81], off
	v_mfma_f32_16x16x32_f16 v[32:35], v[116:119], v[148:151], v[32:35]
	v_mfma_f32_16x16x32_f16 v[24:27], v[124:127], v[148:151], v[24:27]
	v_mfma_f32_16x16x32_f16 v[16:19], v[116:119], v[156:159], v[16:19]
	v_mfma_f32_16x16x32_f16 v[0:3], v[124:127], v[156:159], v[0:3]
	v_mfma_f32_16x16x32_f16 v[32:35], v[120:123], v[152:155], v[32:35]
	v_mfma_f32_16x16x32_f16 v[24:27], v[128:131], v[152:155], v[24:27]
	v_mfma_f32_16x16x32_f16 v[16:19], v[120:123], v[160:163], v[16:19]
	v_mfma_f32_16x16x32_f16 v[0:3], v[128:131], v[160:163], v[0:3]
	s_setprio 0
	s_add_i32 s7, s7, 1
	s_cmp_lg_u32 s7, 16
	s_cselect_b32 s7, s7, 0
	s_barrier
	s_add_i32 s13, s13, -1
	s_mov_b32 s17, s10
	s_mov_b32 s10, s14
	s_cmp_lg_u32 s13, 0
	s_mov_b32 s14, s15
	s_cbranch_scc1 .LBB1_7
	s_sub_u32 s0, s0, s8
	s_subb_u32 s1, s1, s9
	s_add_u32 s0, s8, s0
	s_addc_u32 s1, s9, s1
	s_lshl_b32 s3, s3, 6
	s_or_b32 s3, s3, s16
	s_lshl_b32 s4, s6, 1
	v_lshrrev_b32_e32 v86, 5, v106
	v_pk_add_f32 v[78:79], v[22:23], v[78:79]
	v_pk_add_f32 v[76:77], v[20:21], v[76:77]
	v_pk_add_f32 v[72:73], v[12:13], v[72:73]
	s_or_b32 s3, s3, s4
	s_lshl_b32 s2, s2, 6
	v_cvt_pk_f16_f32 v76, v76, v77
	v_cvt_pk_f16_f32 v77, v78, v79
	v_cvt_pk_f16_f32 v78, v72, v73
	v_or_b32_e32 v72, s3, v86
	s_or_b32 s2, s2, s16
	v_ashrrev_i32_e32 v73, 31, v72
	v_pk_add_f32 v[70:71], v[10:11], v[70:71]
	v_pk_add_f32 v[68:69], v[8:9], v[68:69]
	v_pk_add_f32 v[60:61], v[4:5], v[60:61]
	s_or_b32 s2, s2, s4
	v_lshlrev_b64 v[72:73], 12, v[72:73]
	v_cvt_pk_f16_f32 v68, v68, v69
	v_cvt_pk_f16_f32 v69, v70, v71
	v_cvt_pk_f16_f32 v70, v60, v61
	v_or_b32_e32 v60, s2, v86
	v_mov_b32_e32 v91, 0
	v_pk_add_f32 v[74:75], v[14:15], v[74:75]
	v_lshl_add_u64 v[72:73], s[0:1], 0, v[72:73]
	v_ashrrev_i32_e32 v61, 31, v60
	v_cvt_pk_f16_f32 v79, v74, v75
	v_lshl_add_u64 v[74:75], v[72:73], 0, v[90:91]
	v_lshlrev_b64 v[60:61], 12, v[60:61]
	v_lshl_or_b32 v84, v102, 6, v100
	v_mov_b32_e32 v85, v91
	global_store_dwordx4 v[74:75], v[76:79], off sc1
	v_lshl_add_u64 v[74:75], s[0:1], 0, v[60:61]
	v_pk_add_f32 v[50:51], v[10:11], v[50:51]
	v_pk_add_f32 v[48:49], v[8:9], v[48:49]
	v_pk_add_f32 v[42:43], v[6:7], v[42:43]
	v_pk_add_f32 v[40:41], v[4:5], v[40:41]
	v_pk_add_f32 v[62:63], v[6:7], v[62:63]
	v_cvt_pk_f16_f32 v48, v48, v49
	v_cvt_pk_f16_f32 v49, v50, v51
	v_cvt_pk_f16_f32 v50, v40, v41
	v_cvt_pk_f16_f32 v51, v42, v43
	v_lshl_add_u64 v[40:41], v[74:75], 0, v[84:85]
	v_cvt_pk_f16_f32 v71, v62, v63
	v_lshl_add_u64 v[60:61], v[74:75], 0, v[90:91]
	global_store_dwordx4 v[40:41], v[48:51], off sc1
	v_pk_add_f32 v[42:43], v[22:23], v[54:55]
	v_pk_add_f32 v[40:41], v[20:21], v[52:53]
	v_lshl_or_b32 v80, v103, 6, v100
	v_lshl_or_b32 v82, v104, 6, v100
	v_mov_b32_e32 v81, v91
	v_mov_b32_e32 v83, v91
	global_store_dwordx4 v[60:61], v[68:71], off sc1
	v_pk_add_f32 v[62:63], v[22:23], v[66:67]
	v_pk_add_f32 v[60:61], v[20:21], v[64:65]
	v_pk_add_f32 v[58:59], v[14:15], v[58:59]
	v_pk_add_f32 v[56:57], v[12:13], v[56:57]
	v_cvt_pk_f16_f32 v40, v40, v41
	v_cvt_pk_f16_f32 v41, v42, v43
	v_pk_add_f32 v[46:47], v[14:15], v[46:47]
	v_pk_add_f32 v[42:43], v[12:13], v[44:45]
	v_pk_add_f32 v[34:35], v[10:11], v[34:35]
	v_pk_add_f32 v[32:33], v[8:9], v[32:33]
	v_pk_add_f32 v[26:27], v[6:7], v[26:27]
	v_pk_add_f32 v[24:25], v[4:5], v[24:25]
	v_pk_add_f32 v[22:23], v[22:23], v[38:39]
	v_pk_add_f32 v[20:21], v[20:21], v[36:37]
	v_pk_add_f32 v[14:15], v[14:15], v[30:31]
	v_pk_add_f32 v[12:13], v[12:13], v[28:29]
	v_pk_add_f32 v[10:11], v[10:11], v[18:19]
	v_pk_add_f32 v[8:9], v[8:9], v[16:17]
	v_pk_add_f32 v[2:3], v[6:7], v[2:3]
	v_pk_add_f32 v[0:1], v[4:5], v[0:1]
	v_cvt_pk_f16_f32 v60, v60, v61
	v_cvt_pk_f16_f32 v61, v62, v63
	v_cvt_pk_f16_f32 v62, v56, v57
	v_cvt_pk_f16_f32 v63, v58, v59
	v_lshl_add_u64 v[56:57], v[72:73], 0, v[84:85]
	v_cvt_pk_f16_f32 v42, v42, v43
	v_cvt_pk_f16_f32 v43, v46, v47
	v_lshl_add_u64 v[44:45], v[72:73], 0, v[80:81]
	v_cvt_pk_f16_f32 v32, v32, v33
	v_cvt_pk_f16_f32 v33, v34, v35
	v_cvt_pk_f16_f32 v34, v24, v25
	v_cvt_pk_f16_f32 v35, v26, v27
	v_lshl_add_u64 v[24:25], v[74:75], 0, v[80:81]
	v_cvt_pk_f16_f32 v20, v20, v21
	v_cvt_pk_f16_f32 v21, v22, v23
	v_cvt_pk_f16_f32 v22, v12, v13
	v_cvt_pk_f16_f32 v23, v14, v15
	v_lshl_add_u64 v[12:13], v[72:73], 0, v[82:83]
	v_cvt_pk_f16_f32 v8, v8, v9
	v_cvt_pk_f16_f32 v9, v10, v11
	v_cvt_pk_f16_f32 v10, v0, v1
	v_cvt_pk_f16_f32 v11, v2, v3
	v_lshl_add_u64 v[0:1], v[74:75], 0, v[82:83]
	global_store_dwordx4 v[56:57], v[60:63], off sc1
	global_store_dwordx4 v[44:45], v[40:43], off sc1
	global_store_dwordx4 v[24:25], v[32:35], off sc1
	global_store_dwordx4 v[12:13], v[20:23], off sc1
	global_store_dwordx4 v[0:1], v[8:11], off sc1
	s_waitcnt vmcnt(0)
	s_cmpk_gt_u32 s18, 0xff
	s_cbranch_scc1 .LBB1_10
	s_barrier

.LBB2_3:
	s_mov_b32 s16, s15
	v_add_u32_e32 v116, s16, v87
	v_add_u32_e32 v148, s16, v0
	ds_read_b128 v[88:91], v116 offset:16384
	ds_read_b128 v[92:95], v116 offset:17408
	ds_read_b128 v[96:99], v116 offset:18432
	ds_read_b128 v[100:103], v116 offset:19456
	ds_read_b128 v[104:107], v116 offset:32768
	ds_read_b128 v[108:111], v116 offset:33792
	ds_read_b128 v[112:115], v116 offset:34816
	ds_read_b128 v[116:119], v116 offset:35840
	ds_read_b128 v[120:123], v148
	ds_read_b128 v[124:127], v148 offset:1024
	ds_read_b128 v[128:131], v148 offset:2048
	ds_read_b128 v[132:135], v148 offset:3072
	ds_read_b128 v[136:139], v148 offset:4096
	ds_read_b128 v[140:143], v148 offset:5120
	ds_read_b128 v[144:147], v148 offset:6144
	ds_read_b128 v[148:151], v148 offset:7168
	s_lshl_b32 s15, s7, 7
	s_ashr_i32 s17, s15, 31
	s_add_u32 s18, s4, s15
	s_addc_u32 s19, s5, s17
	s_add_u32 s20, s2, s15
	s_addc_u32 s21, s3, s17
	s_add_i32 s15, s6, s14
	v_lshl_add_u64 v[152:153], s[18:19], 0, v[82:83]
	s_add_i32 m0, s15, 0x4000
	s_nop 0
	global_load_lds_dwordx4 v[152:153], off
	v_lshl_add_u64 v[152:153], s[18:19], 0, v[84:85]
	s_add_i32 m0, s15, 0x6000
	s_nop 0
	global_load_lds_dwordx4 v[152:153], off
	v_lshl_add_u64 v[152:153], s[20:21], 0, v[82:83]
	s_mov_b32 m0, s15
	s_nop 0
	global_load_lds_dwordx4 v[152:153], off
	s_waitcnt vmcnt(3)
	s_waitcnt lgkmcnt(0)
	s_barrier
	s_setprio 1
	s_waitcnt lgkmcnt(0)
	v_mfma_f32_16x16x32_f16 v[18:21], v[88:91], v[120:123], v[18:21]
	v_mfma_f32_16x16x32_f16 v[70:73], v[96:99], v[120:123], v[70:73]
	v_mfma_f32_16x16x32_f16 v[58:61], v[88:91], v[128:131], v[58:61]
	v_mfma_f32_16x16x32_f16 v[54:57], v[96:99], v[128:131], v[54:57]
	v_mfma_f32_16x16x32_f16 v[18:21], v[92:95], v[124:127], v[18:21]
	v_mfma_f32_16x16x32_f16 v[70:73], v[100:103], v[124:127], v[70:73]
	v_mfma_f32_16x16x32_f16 v[58:61], v[92:95], v[132:135], v[58:61]
	v_mfma_f32_16x16x32_f16 v[54:57], v[100:103], v[132:135], v[54:57]
	s_add_u32 s18, s18, 0x40000
	s_addc_u32 s19, s19, 0
	v_lshl_add_u64 v[152:153], s[18:19], 0, v[82:83]
	s_add_i32 m0, s15, 0x8000
	s_nop 0
	global_load_lds_dwordx4 v[152:153], off
	v_mfma_f32_16x16x32_f16 v[42:45], v[88:91], v[136:139], v[42:45]
	v_mfma_f32_16x16x32_f16 v[38:41], v[96:99], v[136:139], v[38:41]
	v_mfma_f32_16x16x32_f16 v[26:29], v[88:91], v[144:147], v[26:29]
	v_mfma_f32_16x16x32_f16 v[22:25], v[96:99], v[144:147], v[22:25]
	v_mfma_f32_16x16x32_f16 v[42:45], v[92:95], v[140:143], v[42:45]
	v_mfma_f32_16x16x32_f16 v[38:41], v[100:103], v[140:143], v[38:41]
	v_mfma_f32_16x16x32_f16 v[26:29], v[92:95], v[148:151], v[26:29]
	v_mfma_f32_16x16x32_f16 v[22:25], v[100:103], v[148:151], v[22:25]
	v_lshl_add_u64 v[88:89], s[18:19], 0, v[84:85]
	s_add_i32 m0, s15, 0xa000
	s_nop 0
	global_load_lds_dwordx4 v[88:89], off
	v_mfma_f32_16x16x32_f16 v[78:81], v[104:107], v[120:123], v[78:81]
	v_mfma_f32_16x16x32_f16 v[74:77], v[112:115], v[120:123], v[74:77]
	v_mfma_f32_16x16x32_f16 v[66:69], v[104:107], v[128:131], v[66:69]
	v_mfma_f32_16x16x32_f16 v[62:65], v[112:115], v[128:131], v[62:65]
	v_mfma_f32_16x16x32_f16 v[78:81], v[108:111], v[124:127], v[78:81]
	v_mfma_f32_16x16x32_f16 v[74:77], v[116:119], v[124:127], v[74:77]
	v_mfma_f32_16x16x32_f16 v[66:69], v[108:111], v[132:135], v[66:69]
	v_mfma_f32_16x16x32_f16 v[62:65], v[116:119], v[132:135], v[62:65]
	v_lshl_add_u64 v[88:89], s[20:21], 0, v[84:85]
	s_add_i32 m0, s15, 0x2000
	s_nop 0
	global_load_lds_dwordx4 v[88:89], off
	v_mfma_f32_16x16x32_f16 v[50:53], v[104:107], v[136:139], v[50:53]
	v_mfma_f32_16x16x32_f16 v[46:49], v[112:115], v[136:139], v[46:49]
	v_mfma_f32_16x16x32_f16 v[34:37], v[104:107], v[144:147], v[34:37]
	v_mfma_f32_16x16x32_f16 v[30:33], v[112:115], v[144:147], v[30:33]
	v_mfma_f32_16x16x32_f16 v[50:53], v[108:111], v[140:143], v[50:53]
	v_mfma_f32_16x16x32_f16 v[46:49], v[116:119], v[140:143], v[46:49]
	v_mfma_f32_16x16x32_f16 v[34:37], v[108:111], v[148:151], v[34:37]
	v_mfma_f32_16x16x32_f16 v[30:33], v[116:119], v[148:151], v[30:33]
	s_setprio 0
	s_add_i32 s7, s7, 1
	s_cmp_lg_u32 s7, 16
	s_cselect_b32 s7, s7, 0
	s_barrier
	s_add_i32 s11, s11, -1
	s_mov_b32 s15, s13
	s_mov_b32 s13, s14
	s_cmp_lg_u32 s11, 0
	s_mov_b32 s14, s16
	s_cbranch_scc1 .LBB2_3
	v_lshl_add_u32 v0, s0, 7, v86
	v_or_b32_e32 v88, s10, v1
	v_ashrrev_i32_e32 v1, 31, v0
	v_lshlrev_b64 v[82:83], 12, v[0:1]
	v_or_b32_e32 v88, s1, v88
	v_lshl_add_u64 v[82:83], s[8:9], 0, v[82:83]
	v_lshlrev_b32_e32 v88, 2, v88
	v_mov_b32_e32 v89, 0
	v_or_b32_e32 v84, 16, v0
	v_lshl_add_u64 v[82:83], v[82:83], 0, v[88:89]
	v_pk_add_f32 v[20:21], v[16:17], v[20:21]
	v_pk_add_f32 v[18:19], v[14:15], v[18:19]
	v_ashrrev_i32_e32 v85, 31, v84
	global_store_dwordx4 v[82:83], v[18:21], off sc1
	v_lshlrev_b64 v[84:85], 12, v[84:85]
	v_lshl_add_u64 v[84:85], s[8:9], 0, v[84:85]
	v_pk_add_f32 v[20:21], v[12:13], v[72:73]
	v_pk_add_f32 v[18:19], v[10:11], v[70:71]
	global_store_dwordx4 v[82:83], v[18:21], off offset:64 sc1
	v_or_b32_e32 v86, 32, v0
	v_lshl_add_u64 v[84:85], v[84:85], 0, v[88:89]
	v_pk_add_f32 v[20:21], v[8:9], v[80:81]
	v_pk_add_f32 v[18:19], v[6:7], v[78:79]
	global_store_dwordx4 v[82:83], v[18:21], off offset:512 sc1
	v_ashrrev_i32_e32 v87, 31, v86
	v_lshlrev_b64 v[86:87], 12, v[86:87]
	v_pk_add_f32 v[20:21], v[4:5], v[76:77]
	v_pk_add_f32 v[18:19], v[2:3], v[74:75]
	global_store_dwordx4 v[82:83], v[18:21], off offset:576 sc1
	v_lshl_add_u64 v[86:87], s[8:9], 0, v[86:87]
	v_or_b32_e32 v0, 48, v0
	v_pk_add_f32 v[20:21], v[16:17], v[60:61]
	v_pk_add_f32 v[18:19], v[14:15], v[58:59]
	global_store_dwordx4 v[84:85], v[18:21], off sc1
	v_ashrrev_i32_e32 v1, 31, v0
	v_lshl_add_u64 v[86:87], v[86:87], 0, v[88:89]
	v_pk_add_f32 v[20:21], v[12:13], v[56:57]
	v_pk_add_f32 v[18:19], v[10:11], v[54:55]
	global_store_dwordx4 v[84:85], v[18:21], off offset:64 sc1
	v_lshlrev_b64 v[0:1], 12, v[0:1]
	v_lshl_add_u64 v[0:1], s[8:9], 0, v[0:1]
	v_pk_add_f32 v[20:21], v[8:9], v[68:69]
	v_pk_add_f32 v[18:19], v[6:7], v[66:67]
	global_store_dwordx4 v[84:85], v[18:21], off offset:512 sc1
	v_lshl_add_u64 v[0:1], v[0:1], 0, v[88:89]
	s_cmpk_gt_u32 s12, 0xff
	v_pk_add_f32 v[20:21], v[4:5], v[64:65]
	v_pk_add_f32 v[18:19], v[2:3], v[62:63]
	global_store_dwordx4 v[84:85], v[18:21], off offset:576 sc1
	s_nop 1
	v_pk_add_f32 v[20:21], v[16:17], v[44:45]
	v_pk_add_f32 v[18:19], v[14:15], v[42:43]
	global_store_dwordx4 v[86:87], v[18:21], off sc1
	v_pk_add_f32 v[16:17], v[16:17], v[28:29]
	v_pk_add_f32 v[14:15], v[14:15], v[26:27]
	v_pk_add_f32 v[20:21], v[12:13], v[40:41]
	v_pk_add_f32 v[18:19], v[10:11], v[38:39]
	global_store_dwordx4 v[86:87], v[18:21], off offset:64 sc1
	v_pk_add_f32 v[12:13], v[12:13], v[24:25]
	v_pk_add_f32 v[10:11], v[10:11], v[22:23]
	v_pk_add_f32 v[20:21], v[8:9], v[52:53]
	v_pk_add_f32 v[18:19], v[6:7], v[50:51]
	global_store_dwordx4 v[86:87], v[18:21], off offset:512 sc1
	v_pk_add_f32 v[8:9], v[8:9], v[36:37]
	v_pk_add_f32 v[6:7], v[6:7], v[34:35]
	v_pk_add_f32 v[20:21], v[4:5], v[48:49]
	v_pk_add_f32 v[18:19], v[2:3], v[46:47]
	v_pk_add_f32 v[4:5], v[4:5], v[32:33]
	v_pk_add_f32 v[2:3], v[2:3], v[30:31]
	global_store_dwordx4 v[86:87], v[18:21], off offset:576 sc1
	global_store_dwordx4 v[0:1], v[14:17], off sc1
	global_store_dwordx4 v[0:1], v[10:13], off offset:64 sc1
	global_store_dwordx4 v[0:1], v[6:9], off offset:512 sc1
	global_store_dwordx4 v[0:1], v[2:5], off offset:576 sc1
	s_waitcnt vmcnt(0)
	s_cbranch_scc1 .LBB2_6
	s_barrier

.LBB3_1:
	s_or_b64 exec, exec, s[2:3]
	s_waitcnt lgkmcnt(0)
	ds_read_b128 v[50:53], v82 offset:49280
	ds_read_b128 v[54:57], v82 offset:49312
	s_add_u32 s2, s16, s36
	s_addc_u32 s3, s17, 0
	s_add_u32 s2, s2, s37
	s_waitcnt lgkmcnt(1)
	v_rcp_f32_e32 v58, v50
	v_rcp_f32_e32 v59, v51
	s_addc_u32 s3, s3, 0
	s_lshl_b32 s12, s35, 12
	v_rcp_f32_e32 v60, v52
	s_add_i32 s12, s12, 0
	v_lshlrev_b32_e32 v66, 1, v1
	v_add3_u32 v66, s12, v66, v231
	v_fma_mixlo_f16 v18, v18, v58, 0
	v_rcp_f32_e32 v61, v53
	ds_write_b16 v66, v18 offset:51264
	v_fma_mixlo_f16 v18, v35, v59, 0
	ds_write_b16 v66, v18 offset:51328
	v_fma_mixlo_f16 v18, v19, v59, 0
	s_waitcnt lgkmcnt(2)
	v_rcp_f32_e32 v62, v54
	ds_write_b16 v66, v18 offset:51392
	v_fma_mixlo_f16 v18, v36, v60, 0
	ds_write_b16 v66, v18 offset:51456
	v_fma_mixlo_f16 v18, v20, v60, 0
	v_rcp_f32_e32 v63, v55
	ds_write_b16 v66, v18 offset:51520
	v_fma_mixlo_f16 v18, v37, v61, 0
	ds_read_b128 v[50:53], v82 offset:49344
	ds_write_b16 v66, v18 offset:51584
	v_fma_mixlo_f16 v18, v21, v61, 0
	v_rcp_f32_e32 v64, v56
	ds_write_b16 v66, v18 offset:51648
	v_fma_mixlo_f16 v18, v38, v62, 0
	ds_write_b16 v66, v18 offset:52224
	v_fma_mixlo_f16 v18, v22, v62, 0
	v_rcp_f32_e32 v65, v57
	ds_write_b16 v66, v18 offset:52288
	v_fma_mixlo_f16 v18, v39, v63, 0
	ds_write_b16 v66, v18 offset:52352
	v_fma_mixlo_f16 v18, v23, v63, 0
	ds_read_b128 v[54:57], v82 offset:49376
	s_waitcnt lgkmcnt(6)
	v_rcp_f32_e32 v50, v50
	ds_write_b16 v66, v18 offset:52416
	v_fma_mixlo_f16 v18, v40, v64, 0
	ds_write_b16 v66, v18 offset:52480
	v_fma_mixlo_f16 v18, v24, v64, 0
	v_rcp_f32_e32 v51, v51
	ds_write_b16 v66, v18 offset:52544
	v_fma_mixlo_f16 v18, v41, v65, 0
	ds_write_b16 v66, v18 offset:52608
	v_fma_mixlo_f16 v18, v25, v65, 0
	v_rcp_f32_e32 v52, v52
	ds_write_b16 v66, v18 offset:52672
	v_fma_mixlo_f16 v18, v42, v50, 0
	ds_write_b16 v66, v18 offset:53248
	v_fma_mixlo_f16 v18, v26, v50, 0
	v_rcp_f32_e32 v53, v53
	ds_write_b16 v66, v18 offset:53312
	v_fma_mixlo_f16 v18, v43, v51, 0
	ds_write_b16 v66, v18 offset:53376
	v_fma_mixlo_f16 v18, v27, v51, 0
	s_waitcnt lgkmcnt(8)
	v_rcp_f32_e32 v54, v54
	ds_write_b16 v66, v18 offset:53440
	v_fma_mixlo_f16 v18, v44, v52, 0
	ds_write_b16 v66, v18 offset:53504
	v_fma_mixlo_f16 v18, v28, v52, 0
	v_rcp_f32_e32 v55, v55
	ds_write_b16 v66, v18 offset:53568
	v_fma_mixlo_f16 v18, v45, v53, 0
	ds_write_b16 v66, v18 offset:53632
	v_fma_mixlo_f16 v18, v29, v53, 0
	v_rcp_f32_e32 v56, v56
	ds_write_b16 v66, v18 offset:53696
	v_fma_mixlo_f16 v18, v46, v54, 0
	ds_write_b16 v66, v18 offset:54272
	v_fma_mixlo_f16 v18, v30, v54, 0
	v_rcp_f32_e32 v57, v57
	ds_write_b16 v66, v18 offset:54336
	v_fma_mixlo_f16 v18, v47, v55, 0
	ds_write_b16 v66, v18 offset:54400
	v_fma_mixlo_f16 v18, v31, v55, 0
	ds_write_b16 v66, v18 offset:54464
	v_fma_mixlo_f16 v18, v48, v56, 0
	ds_write_b16 v66, v18 offset:54528
	v_fma_mixlo_f16 v18, v32, v56, 0
	ds_write_b16 v66, v18 offset:54592
	v_fma_mixlo_f16 v18, v49, v57, 0
	v_fma_mixlo_f16 v34, v34, v58, 0
	ds_write_b16 v66, v18 offset:54656
	v_fma_mixlo_f16 v18, v33, v57, 0
	ds_write_b16 v66, v34 offset:51200
	ds_write_b16 v66, v18 offset:54720
	v_lshl_add_u32 v30, v232, 1, s12
	s_waitcnt lgkmcnt(0)
	v_add_u32_e32 v18, v30, v233
	ds_read_b128 v[18:21], v18 offset:51200
	v_add_u32_e32 v22, v30, v234
	ds_read_b128 v[22:25], v22 offset:51200
	s_lshl_b64 s[2:3], s[2:3], 11
	v_lshl_add_u64 v[26:27], v[214:215], 0, s[2:3]
	v_lshl_add_u64 v[28:29], v[26:27], 0, v[206:207]
	v_mov_b32_e32 v217, v207
	s_waitcnt lgkmcnt(1)
	global_store_dwordx4 v[28:29], v[18:21], off sc1
	v_mov_b32_e32 v219, v207
	v_lshl_add_u64 v[28:29], v[26:27], 0, v[218:219]
	v_lshl_add_u64 v[18:19], v[26:27], 0, v[216:217]
	s_waitcnt lgkmcnt(0)
	global_store_dwordx4 v[18:19], v[22:25], off sc1
	v_add_u32_e32 v18, v30, v235
	ds_read_b128 v[18:21], v18 offset:51200
	v_add_u32_e32 v22, v30, v236
	ds_read_b128 v[22:25], v22 offset:51200
	v_mov_b32_e32 v221, v207
	s_mov_b64 s[2:3], 0
	s_waitcnt lgkmcnt(1)
	global_store_dwordx4 v[28:29], v[18:21], off sc1
	s_andn2_b64 vcc, exec, s[22:23]
	s_mov_b32 s26, s33
	v_lshl_add_u64 v[18:19], v[26:27], 0, v[220:221]
	s_waitcnt lgkmcnt(0)
	global_store_dwordx4 v[18:19], v[22:25], off sc1
	s_waitcnt lgkmcnt(0)
	s_barrier
	s_cbranch_vccz .LBB3_80
